# band tile loop: 13 v_pk_mul_f32 O-rescale split into scalar v_mul_f32 pairs (on top of v28)
# baseline (speedup 1.0000x reference)
.Lband_nopf:
	s_waitcnt lgkmcnt(0)
	s_nop 10
	v_fmamk_f32 v197, v52, 0x3e38aa3b, v199
	v_fmac_f32_e32 v198, 0x3e38aa3b, v53
	ds_read2_b32 v[52:53], v153 offset0:24 offset1:25
	v_max3_f32 v195, v197, s33, v198
	s_waitcnt lgkmcnt(0)
	v_fmamk_f32 v53, v54, 0x3e38aa3b, v53
	v_fmac_f32_e32 v52, 0x3e38aa3b, v55
	ds_read2_b32 v[54:55], v153 offset0:18 offset1:19
	v_max3_f32 v195, v195, v53, v52
	s_waitcnt lgkmcnt(0)
	v_fmamk_f32 v55, v56, 0x3e38aa3b, v55
	v_fmac_f32_e32 v54, 0x3e38aa3b, v57
	ds_read2_b32 v[56:57], v153 offset0:16 offset1:17
	v_max3_f32 v195, v195, v55, v54
	s_waitcnt lgkmcnt(0)
	v_fmamk_f32 v57, v58, 0x3e38aa3b, v57
	v_fmac_f32_e32 v56, 0x3e38aa3b, v59
	ds_read2_b32 v[58:59], v153 offset0:10 offset1:11
	v_max3_f32 v195, v195, v57, v56
	s_waitcnt lgkmcnt(0)
	v_fmamk_f32 v59, v60, 0x3e38aa3b, v59
	v_fmac_f32_e32 v58, 0x3e38aa3b, v61
	ds_read2_b32 v[60:61], v153 offset0:8 offset1:9
	v_max3_f32 v195, v195, v59, v58
	s_waitcnt lgkmcnt(0)
	v_fmamk_f32 v61, v62, 0x3e38aa3b, v61
	v_fmac_f32_e32 v60, 0x3e38aa3b, v63
	ds_read2_b32 v[62:63], v153 offset0:2 offset1:3
	v_max3_f32 v195, v195, v61, v60
	s_waitcnt lgkmcnt(0)
	v_fmamk_f32 v63, v64, 0x3e38aa3b, v63
	v_fmac_f32_e32 v62, 0x3e38aa3b, v65
	ds_read2_b32 v[64:65], v153 offset1:1
	v_max3_f32 v195, v195, v63, v62
	s_waitcnt lgkmcnt(0)
	v_fmamk_f32 v65, v66, 0x3e38aa3b, v65
	v_fmac_f32_e32 v64, 0x3e38aa3b, v67
	v_max3_f32 v66, v195, v65, v64
	v_mov_b32_e32 v67, v66
	s_nop 1
	v_permlane32_swap_b32_e32 v66, v67
	v_max3_f32 v195, v196, v66, v67
	v_sub_f32_e32 v67, v197, v195
	v_exp_f32_e32 v67, v67
	v_sub_f32_e32 v197, v198, v195
	v_exp_f32_e32 v197, v197
	v_sub_f32_e32 v53, v53, v195
	v_exp_f32_e32 v53, v53
	v_sub_f32_e32 v52, v52, v195
	v_exp_f32_e32 v52, v52
	v_sub_f32_e32 v55, v55, v195
	v_sub_f32_e32 v66, v196, v195
	v_add_f32_e32 v196, 0, v67
	v_exp_f32_e32 v55, v55
	v_sub_f32_e32 v54, v54, v195
	v_add_f32_e32 v196, v197, v196
	v_exp_f32_e32 v54, v54
	v_sub_f32_e32 v57, v57, v195
	v_add_f32_e32 v196, v53, v196
	v_exp_f32_e32 v198, v57
	v_add_f32_e32 v196, v52, v196
	v_add_f32_e32 v196, v55, v196
	v_add_f32_e32 v196, v54, v196
	v_sub_f32_e32 v56, v56, v195
	v_add_f32_e32 v57, v198, v196
	v_exp_f32_e32 v196, v56
	s_nop 0
	v_add_f32_e32 v56, v196, v57
	v_sub_f32_e32 v57, v59, v195
	v_exp_f32_e32 v59, v57
	v_sub_f32_e32 v57, v58, v195
	v_exp_f32_e32 v199, v57
	v_sub_f32_e32 v57, v61, v195
	v_exp_f32_e32 v200, v57
	v_sub_f32_e32 v57, v60, v195
	v_exp_f32_e32 v201, v57
	v_sub_f32_e32 v57, v63, v195
	v_add_f32_e32 v56, v59, v56
	v_exp_f32_e32 v202, v57
	v_sub_f32_e32 v57, v62, v195
	v_add_f32_e32 v56, v199, v56
	v_exp_f32_e32 v203, v57
	v_sub_f32_e32 v57, v65, v195
	v_add_f32_e32 v56, v200, v56
	v_exp_f32_e32 v65, v57
	v_sub_f32_e32 v57, v64, v195
	v_add_f32_e32 v56, v201, v56
	v_exp_f32_e32 v64, v57
	v_add_f32_e32 v56, v202, v56
	v_add_f32_e32 v56, v203, v56
	v_add_f32_e32 v56, v65, v56
	v_add_f32_e32 v57, v64, v56
	v_exp_f32_e32 v56, v66
	v_cvt_pk_bf16_f32 v60, v67, v197
	v_cvt_pk_bf16_f32 v62, v55, v54
	v_cvt_pk_bf16_f32 v55, v65, v64
	ds_read_b64_tr_b16 v[64:65], v192 offset:32768
	ds_read_b64_tr_b16 v[66:67], v192 offset:33280
	v_mov_b32_e32 v58, v57
	s_nop 1
	v_permlane32_swap_b32_e32 v57, v58
	v_mul_f32_e32 v34, v56, v34
	v_mul_f32_e32 v35, v56, v35
	v_mul_f32_e32 v32, v56, v32
	v_mul_f32_e32 v33, v56, v33
	v_mul_f32_e32 v30, v56, v30
	v_mul_f32_e32 v31, v56, v31
	v_mul_f32_e32 v28, v56, v28
	v_mul_f32_e32 v29, v56, v29
	v_mul_f32_e32 v26, v56, v26
	v_mul_f32_e32 v27, v56, v27
	v_mul_f32_e32 v24, v56, v24
	v_mul_f32_e32 v25, v56, v25
	v_mul_f32_e32 v22, v56, v22
	v_mul_f32_e32 v23, v56, v23
	v_mul_f32_e32 v20, v56, v20
	v_mul_f32_e32 v21, v56, v21
	v_cvt_pk_bf16_f32 v61, v53, v52
	v_cvt_pk_bf16_f32 v63, v198, v196
	v_cvt_pk_bf16_f32 v52, v59, v199
	v_cvt_pk_bf16_f32 v53, v200, v201
	v_cvt_pk_bf16_f32 v54, v202, v203
	v_mul_f32_e32 v50, v56, v50
	v_mul_f32_e32 v51, v56, v51
	s_waitcnt lgkmcnt(0)
	v_mfma_f32_32x32x16_bf16 v[20:35], v[64:67], v[60:63], v[20:35]
	ds_read_b64_tr_b16 v[64:65], v192 offset:33792
	ds_read_b64_tr_b16 v[66:67], v192 offset:34304
	v_mul_f32_e64 v48, v48, v56
	v_mul_f32_e64 v49, v49, v56
	v_mul_f32_e64 v46, v46, v56
	v_mul_f32_e64 v47, v47, v56
	v_mul_f32_e32 v44, v56, v44
	v_mul_f32_e32 v45, v56, v45
	v_mul_f32_e32 v42, v56, v42
	v_mul_f32_e32 v43, v56, v43
	v_mul_f32_e32 v40, v56, v40
	v_mul_f32_e32 v41, v56, v41
	v_mul_f32_e32 v38, v56, v38
	v_mul_f32_e32 v39, v56, v39
	s_waitcnt lgkmcnt(0)
	v_mfma_f32_32x32x16_bf16 v[20:35], v[64:67], v[52:55], v[20:35]
	ds_read_b64_tr_b16 v[64:65], v192 offset:34816
	ds_read_b64_tr_b16 v[66:67], v192 offset:35328
	v_mul_f32_e64 v36, v36, v56
	v_mul_f32_e64 v37, v37, v56
	s_waitcnt lgkmcnt(0)
	s_nop 0
	v_mfma_f32_32x32x16_bf16 v[36:51], v[64:67], v[60:63], v[36:51]
	ds_read_b64_tr_b16 v[60:61], v192 offset:35840
	ds_read_b64_tr_b16 v[62:63], v192 offset:36352
	s_waitcnt lgkmcnt(0)
	v_mfma_f32_32x32x16_bf16 v[36:51], v[60:63], v[52:55], v[36:51]
